# P + attention main loop: the loop-invariant barrier flag at the MFMA segment's tail is computed by one s_not_b64 (+ s_nop 0, same wait-state count) instead of v_cndmask + v_cmp
# speedup vs baseline: 1.0254x; 1.0097x over previous
.LBB0_1614:
	s_mul_i32 s14, s13, 0x3400
	s_and_b32 s7, 1, s18
	s_add_i32 s14, s14, 0
	s_andn2_b32 s15, 1, s18
	s_mul_i32 s6, s17, 0x3400
	s_cmpk_lt_u32 s18, 0xfc
	s_cselect_b32 s21, s20, 0x2fd000
	s_cmp_eq_u32 s7, 1
	v_add_u32_e32 v96, s14, v199
	s_waitcnt lgkmcnt(6)
	v_mfma_scale_f32_32x32x64_f8f6f4 v[80:95], v[168:175], v[136:143], v[64:79], v191, v190 op_sel_hi:[0,0,0]
	s_waitcnt vmcnt(2)
	ds_write_b128 v96, v[180:183] offset:20480
	v_add_u32_e32 v96, s14, v200
	s_mulk_i32 s15, 0x2800
	s_waitcnt vmcnt(1)
	ds_write_b64 v96, v[188:189] offset:28672
	v_add_u32_e32 v96, s15, v205
	s_mov_b32 s39, s31
	s_waitcnt vmcnt(0)
	ds_write_b128 v96, v[176:179]
	buffer_load_dwordx4 v[180:183], v203, s[28:31], s21 offen
	buffer_load_dwordx2 v[188:189], v202, s[28:31], s21 offen
	buffer_load_dwordx4 v[176:179], v203, s[36:39], s19 offen
	v_add_u32_e32 v172, s6, v204
	s_cselect_b32 s6, 0x2800, 0
	v_add_u32_e32 v186, s6, v198
	s_waitcnt lgkmcnt(7)
	v_mfma_scale_f32_32x32x64_f8f6f4 v[96:111], v[160:167], v[136:143], v[64:79], v191, v190 op_sel_hi:[0,0,0]
	ds_read_b128 v[160:163], v172 offset:20608
	ds_read_b128 v[164:167], v172 offset:20624
	ds_read_b128 v[168:171], v172 offset:27264
	ds_read_b128 v[172:175], v172 offset:27280
	s_waitcnt lgkmcnt(9)
	v_mfma_scale_f32_32x32x64_f8f6f4 v[80:95], v[152:159], v[128:135], v[80:95], v191, v190 op_sel_hi:[0,0,0]
	ds_read_b128 v[152:155], v186
	ds_read_b128 v[156:159], v186 offset:16
	ds_read_b128 v[206:209], v186 offset:2560
	ds_read_b128 v[210:213], v186 offset:2576
	s_waitcnt lgkmcnt(11)
	v_mfma_scale_f32_32x32x64_f8f6f4 v[96:111], v[144:151], v[128:135], v[96:111], v191, v190 op_sel_hi:[0,0,0]
	ds_read_b128 v[144:147], v186 offset:5120
	ds_read_b128 v[148:151], v186 offset:5136
	ds_read_b128 v[214:217], v186 offset:7680
	ds_read_b128 v[218:221], v186 offset:7696
	s_waitcnt lgkmcnt(10)
	v_mfma_scale_f32_32x32x64_f8f6f4 v[80:95], v[160:167], v[120:127], v[80:95], v191, v190 op_sel_hi:[0,0,0]
	s_waitcnt lgkmcnt(8)
	v_mfma_scale_f32_32x32x64_f8f6f4 v[96:111], v[168:175], v[120:127], v[96:111], v191, v190 op_sel_hi:[0,0,0]
	s_waitcnt lgkmcnt(6)
	v_mfma_f32_32x32x64_f8f6f4 v[0:15], v[112:119], v[152:159], v[0:15]
	s_waitcnt lgkmcnt(4)
	v_mfma_f32_32x32x64_f8f6f4 v[16:31], v[112:119], v[206:213], v[16:31]
	s_waitcnt lgkmcnt(2)
	v_mfma_f32_32x32x64_f8f6f4 v[32:47], v[112:119], v[144:151], v[32:47]
	s_waitcnt lgkmcnt(0)
	v_mfma_f32_32x32x64_f8f6f4 v[48:63], v[112:119], v[214:221], v[48:63]
	s_not_b64 s[6:7], s[46:47]
	s_nop 0
	s_andn2_b64 vcc, exec, s[46:47]
	s_cbranch_vccnz .LBB0_1616
	s_barrier
